# hot/cold code layout: overflow radix fallback and short-count score path moved behind the query loop back branch (I-cache footprint 56->46 KB)
# baseline (speedup 1.0000x reference)
.LBB0_740:
	v_cmp_lt_u32_e32 vcc, 20, v91
	s_cbranch_vccnz .Lcold_ovf

.Lpad_skip:
	s_add_i32 s0, s97, s25
	s_ashr_i32 s1, s0, 31
	s_waitcnt lgkmcnt(0)
	s_lshl_b64 s[8:9], s[0:1], 10
	v_readlane_b32 s14, v254, 60
	v_lshl_add_u32 v2, v210, 1, s95
	v_ashrrev_i32_e32 v213, 3, v10
	v_and_b32_e32 v214, 7, v10
	s_add_u32 s8, s14, s8
	v_readlane_b32 s14, v254, 61
	v_and_b32_e32 v120, 7, v210
	ds_read_u16 v15, v2
	ds_read_u16 v32, v2 offset:32
	ds_read_u16 v38, v2 offset:64
	ds_read_u16 v39, v2 offset:96
	ds_read_u16 v40, v2 offset:128
	ds_read_u16 v41, v2 offset:160
	ds_read_u16 v54, v2 offset:192
	ds_read_u16 v55, v2 offset:224
	ds_read_u16 v56, v2 offset:256
	ds_read_u16 v14, v2 offset:288
	ds_read_u16 v13, v2 offset:320
	ds_read_u16 v12, v2 offset:352
	ds_read_u16 v9, v2 offset:384
	ds_read_u16 v8, v2 offset:416
	ds_read_u16 v7, v2 offset:448
	ds_read_u16 v6, v2 offset:480
	s_addc_u32 s9, s14, s9
	v_lshl_add_u32 v212, v213, 1, s95
	v_lshlrev_b32_e32 v140, 7, v120
	v_lshlrev_b32_e32 v24, 4, v211
	v_lshl_add_u64 v[2:3], s[8:9], 0, v[140:141]
	v_ashrrev_i32_e32 v25, 31, v24
	v_lshl_add_u64 v[2:3], v[24:25], 1, v[2:3]
	global_load_dwordx4 v[16:19], v[2:3], off
	global_load_dwordx4 v[20:23], v[2:3], off offset:16
	ds_read_u16 v5, v212
	ds_read_u16 v4, v212 offset:16
	ds_read_u16 v11, v212 offset:32
	ds_read_u16 v10, v212 offset:48
	s_waitcnt lgkmcnt(0)
	v_lshl_add_u64 v[2:3], s[46:47], 0, v[24:25]
	s_waitcnt lgkmcnt(0)
	v_lshl_add_u32 v244, v15, 7, v24
	global_load_dwordx4 v[156:159], v244, s[46:47]
	global_load_dwordx4 v[160:163], v244, s[46:47] offset:64
	v_lshl_add_u32 v244, v32, 7, v24
	global_load_dwordx4 v[164:167], v244, s[46:47]
	global_load_dwordx4 v[168:171], v244, s[46:47] offset:64
	v_lshl_add_u32 v244, v38, 7, v24
	global_load_dwordx4 v[172:175], v244, s[46:47]
	global_load_dwordx4 v[176:179], v244, s[46:47] offset:64
	v_lshl_add_u32 v244, v39, 7, v24
	global_load_dwordx4 v[180:183], v244, s[46:47]
	global_load_dwordx4 v[184:187], v244, s[46:47] offset:64
	v_lshl_add_u32 v244, v40, 7, v24
	global_load_dwordx4 v[188:191], v244, s[46:47]
	global_load_dwordx4 v[192:195], v244, s[46:47] offset:64
	v_lshl_add_u32 v244, v41, 7, v24
	global_load_dwordx4 v[196:199], v244, s[46:47]
	global_load_dwordx4 v[224:227], v244, s[46:47] offset:64
	v_lshl_add_u32 v244, v54, 7, v24
	global_load_dwordx4 v[228:231], v244, s[46:47]
	global_load_dwordx4 v[232:235], v244, s[46:47] offset:64
	v_lshl_add_u32 v244, v55, 7, v24
	global_load_dwordx4 v[236:239], v244, s[46:47]
	global_load_dwordx4 v[240:243], v244, s[46:47] offset:64
	v_mov_b32_e32 v15, v141
	v_mov_b32_e32 v42, v141
	v_mov_b32_e32 v43, v141
	v_mov_b32_e32 v44, v141
	v_lshlrev_b32_e32 v116, 4, v214
	v_ashrrev_i32_e32 v117, 31, v116
	v_lshl_add_u64 v[114:115], s[48:49], 0, v[116:117]
	v_lshl_add_u32 v121, v211, 3, s95
	v_lshlrev_b32_e32 v117, 2, v211
	ds_read2_b64 v[110:113], v121 offset1:4
	ds_read2_b64 v[106:109], v121 offset0:8 offset1:12
	ds_read2_b64 v[102:105], v121 offset0:16 offset1:20
	ds_read2_b64 v[98:101], v121 offset0:24 offset1:28
	ds_read2_b64 v[94:97], v121 offset0:32 offset1:36
	ds_read2_b64 v[90:93], v121 offset0:40 offset1:44
	ds_read2_b64 v[86:89], v121 offset0:48 offset1:52
	s_waitcnt vmcnt(16)
	v_lshlrev_b32_e32 v45, 16, v16
	v_and_b32_e32 v16, 0xffff0000, v16
	v_lshlrev_b32_e32 v47, 16, v18
	v_and_b32_e32 v18, 0xffff0000, v18
	v_lshlrev_b32_e32 v49, 16, v20
	v_and_b32_e32 v20, 0xffff0000, v20
	v_lshlrev_b32_e32 v51, 16, v22
	v_and_b32_e32 v22, 0xffff0000, v22
	v_mul_f32_e32 v45, 0x41000000, v45
	v_mul_f32_e32 v16, 0x41000000, v16
	v_mul_f32_e32 v47, 0x41000000, v47
	v_mul_f32_e32 v18, 0x41000000, v18
	v_mul_f32_e32 v49, 0x41000000, v49
	v_mul_f32_e32 v20, 0x41000000, v20
	v_mul_f32_e32 v51, 0x41000000, v51
	v_mul_f32_e32 v22, 0x41000000, v22
	v_cvt_pk_fp8_f32 v15, v45, v16
	v_cvt_pk_fp8_f32 v42, v47, v18
	v_cvt_pk_fp8_f32 v43, v49, v20
	v_cvt_pk_fp8_f32 v44, v51, v22
	v_lshlrev_b32_e32 v46, 16, v17
	v_and_b32_e32 v17, 0xffff0000, v17
	v_lshlrev_b32_e32 v48, 16, v19
	v_and_b32_e32 v19, 0xffff0000, v19
	v_lshlrev_b32_e32 v50, 16, v21
	v_and_b32_e32 v21, 0xffff0000, v21
	v_lshlrev_b32_e32 v52, 16, v23
	v_and_b32_e32 v23, 0xffff0000, v23
	v_mul_f32_e32 v46, 0x41000000, v46
	v_mul_f32_e32 v17, 0x41000000, v17
	v_mul_f32_e32 v48, 0x41000000, v48
	v_mul_f32_e32 v19, 0x41000000, v19
	v_mul_f32_e32 v50, 0x41000000, v50
	v_mul_f32_e32 v21, 0x41000000, v21
	v_mul_f32_e32 v52, 0x41000000, v52
	v_mul_f32_e32 v23, 0x41000000, v23
	v_cvt_pk_fp8_f32 v15, v46, v17 op_sel:[0,0,1]
	v_cvt_pk_fp8_f32 v42, v48, v19 op_sel:[0,0,1]
	v_cvt_pk_fp8_f32 v43, v50, v21 op_sel:[0,0,1]
	v_cvt_pk_fp8_f32 v44, v52, v23 op_sel:[0,0,1]
	v_and_b32_e32 v20, -4, v210
	v_cmp_gt_u32_e32 vcc, 4, v210
	s_nop 1
	v_cndmask_b32_e32 v75, 0, v42, vcc
	v_cndmask_b32_e32 v74, 0, v15, vcc
	v_cndmask_b32_e32 v83, 0, v44, vcc
	v_cndmask_b32_e32 v82, 0, v43, vcc
	v_cmp_eq_u32_e32 vcc, 4, v20
	s_nop 1
	v_cndmask_b32_e32 v77, 0, v42, vcc
	v_cndmask_b32_e32 v76, 0, v15, vcc
	v_cndmask_b32_e32 v119, 0, v44, vcc
	v_cndmask_b32_e32 v118, 0, v43, vcc
	s_nop 1
	s_waitcnt vmcnt(14)
	v_mfma_f32_16x16x32_fp8_fp8 v[30:33], v[156:157], v[74:75], 0
	v_mfma_f32_16x16x32_fp8_fp8 v[30:33], v[158:159], v[82:83], v[30:33]
	v_mfma_f32_16x16x32_fp8_fp8 v[30:33], v[160:161], v[76:77], v[30:33]
	v_mfma_f32_16x16x32_fp8_fp8 v[30:33], v[162:163], v[118:119], v[30:33]
	v_lshl_add_u32 v244, v56, 7, v24
	global_load_dwordx4 v[156:159], v244, s[46:47]
	global_load_dwordx4 v[160:163], v244, s[46:47] offset:64
	s_waitcnt vmcnt(14)
	v_mfma_f32_16x16x32_fp8_fp8 v[42:45], v[164:165], v[74:75], 0
	v_mfma_f32_16x16x32_fp8_fp8 v[42:45], v[166:167], v[82:83], v[42:45]
	v_mfma_f32_16x16x32_fp8_fp8 v[42:45], v[168:169], v[76:77], v[42:45]
	v_mfma_f32_16x16x32_fp8_fp8 v[42:45], v[170:171], v[118:119], v[42:45]
	v_lshl_add_u32 v244, v14, 7, v24
	global_load_dwordx4 v[164:167], v244, s[46:47]
	global_load_dwordx4 v[168:171], v244, s[46:47] offset:64
	s_waitcnt vmcnt(14)
	v_mfma_f32_16x16x32_fp8_fp8 v[46:49], v[172:173], v[74:75], 0
	v_mfma_f32_16x16x32_fp8_fp8 v[46:49], v[174:175], v[82:83], v[46:49]
	v_mfma_f32_16x16x32_fp8_fp8 v[46:49], v[176:177], v[76:77], v[46:49]
	v_mfma_f32_16x16x32_fp8_fp8 v[46:49], v[178:179], v[118:119], v[46:49]
	v_lshl_add_u32 v244, v13, 7, v24
	global_load_dwordx4 v[172:175], v244, s[46:47]
	global_load_dwordx4 v[176:179], v244, s[46:47] offset:64
	s_waitcnt vmcnt(14)
	v_mfma_f32_16x16x32_fp8_fp8 v[50:53], v[180:181], v[74:75], 0
	v_mfma_f32_16x16x32_fp8_fp8 v[50:53], v[182:183], v[82:83], v[50:53]
	v_mfma_f32_16x16x32_fp8_fp8 v[50:53], v[184:185], v[76:77], v[50:53]
	v_mfma_f32_16x16x32_fp8_fp8 v[50:53], v[186:187], v[118:119], v[50:53]
	v_lshl_add_u32 v244, v12, 7, v24
	global_load_dwordx4 v[180:183], v244, s[46:47]
	global_load_dwordx4 v[184:187], v244, s[46:47] offset:64
	s_waitcnt vmcnt(14)
	v_mfma_f32_16x16x32_fp8_fp8 v[58:61], v[188:189], v[74:75], 0
	v_mfma_f32_16x16x32_fp8_fp8 v[58:61], v[190:191], v[82:83], v[58:61]
	v_mfma_f32_16x16x32_fp8_fp8 v[58:61], v[192:193], v[76:77], v[58:61]
	v_mfma_f32_16x16x32_fp8_fp8 v[58:61], v[194:195], v[118:119], v[58:61]
	v_lshl_add_u32 v244, v9, 7, v24
	global_load_dwordx4 v[188:191], v244, s[46:47]
	global_load_dwordx4 v[192:195], v244, s[46:47] offset:64
	s_waitcnt vmcnt(14)
	v_mfma_f32_16x16x32_fp8_fp8 v[62:65], v[196:197], v[74:75], 0
	v_mfma_f32_16x16x32_fp8_fp8 v[62:65], v[198:199], v[82:83], v[62:65]
	v_mfma_f32_16x16x32_fp8_fp8 v[62:65], v[224:225], v[76:77], v[62:65]
	v_mfma_f32_16x16x32_fp8_fp8 v[62:65], v[226:227], v[118:119], v[62:65]
	v_lshl_add_u32 v244, v8, 7, v24
	global_load_dwordx4 v[196:199], v244, s[46:47]
	global_load_dwordx4 v[224:227], v244, s[46:47] offset:64
	s_waitcnt vmcnt(14)
	v_mfma_f32_16x16x32_fp8_fp8 v[70:73], v[228:229], v[74:75], 0
	v_mfma_f32_16x16x32_fp8_fp8 v[70:73], v[230:231], v[82:83], v[70:73]
	v_mfma_f32_16x16x32_fp8_fp8 v[70:73], v[232:233], v[76:77], v[70:73]
	v_mfma_f32_16x16x32_fp8_fp8 v[70:73], v[234:235], v[118:119], v[70:73]
	v_lshl_add_u32 v244, v7, 7, v24
	global_load_dwordx4 v[228:231], v244, s[46:47]
	global_load_dwordx4 v[232:235], v244, s[46:47] offset:64
	s_waitcnt vmcnt(14)
	v_mfma_f32_16x16x32_fp8_fp8 v[78:81], v[236:237], v[74:75], 0
	v_mfma_f32_16x16x32_fp8_fp8 v[78:81], v[238:239], v[82:83], v[78:81]
	v_mfma_f32_16x16x32_fp8_fp8 v[78:81], v[240:241], v[76:77], v[78:81]
	v_mfma_f32_16x16x32_fp8_fp8 v[78:81], v[242:243], v[118:119], v[78:81]
	v_lshl_add_u32 v244, v6, 7, v24
	global_load_dwordx4 v[236:239], v244, s[46:47]
	global_load_dwordx4 v[240:243], v244, s[46:47] offset:64
	v_lshl_add_u32 v246, v5, 7, v116
	v_lshl_add_u32 v248, v4, 7, v116
	v_lshl_add_u32 v250, v11, 7, v116
	v_lshl_add_u32 v252, v10, 7, v116
	global_load_dwordx4 v[2:5], v246, s[48:49]
	global_load_dwordx4 v[6:9], v248, s[48:49]
	global_load_dwordx4 v[10:13], v250, s[48:49]
	global_load_dwordx4 v[14:17], v252, s[48:49]
	s_waitcnt vmcnt(18)
	v_mfma_f32_16x16x32_fp8_fp8 v[18:21], v[156:157], v[74:75], 0
	v_mfma_f32_16x16x32_fp8_fp8 v[18:21], v[158:159], v[82:83], v[18:21]
	v_mfma_f32_16x16x32_fp8_fp8 v[18:21], v[160:161], v[76:77], v[18:21]
	v_mfma_f32_16x16x32_fp8_fp8 v[18:21], v[162:163], v[118:119], v[18:21]
	s_waitcnt vmcnt(16)
	v_mfma_f32_16x16x32_fp8_fp8 v[22:25], v[164:165], v[74:75], 0
	v_mfma_f32_16x16x32_fp8_fp8 v[22:25], v[166:167], v[82:83], v[22:25]
	v_mfma_f32_16x16x32_fp8_fp8 v[22:25], v[168:169], v[76:77], v[22:25]
	v_mfma_f32_16x16x32_fp8_fp8 v[22:25], v[170:171], v[118:119], v[22:25]
	s_waitcnt vmcnt(14)
	v_mfma_f32_16x16x32_fp8_fp8 v[26:29], v[172:173], v[74:75], 0
	v_mfma_f32_16x16x32_fp8_fp8 v[26:29], v[174:175], v[82:83], v[26:29]
	v_mfma_f32_16x16x32_fp8_fp8 v[26:29], v[176:177], v[76:77], v[26:29]
	v_mfma_f32_16x16x32_fp8_fp8 v[26:29], v[178:179], v[118:119], v[26:29]
	s_waitcnt vmcnt(12)
	v_mfma_f32_16x16x32_fp8_fp8 v[34:37], v[180:181], v[74:75], 0
	v_mfma_f32_16x16x32_fp8_fp8 v[34:37], v[182:183], v[82:83], v[34:37]
	v_mfma_f32_16x16x32_fp8_fp8 v[34:37], v[184:185], v[76:77], v[34:37]
	v_mfma_f32_16x16x32_fp8_fp8 v[34:37], v[186:187], v[118:119], v[34:37]
	s_waitcnt vmcnt(10)
	v_mfma_f32_16x16x32_fp8_fp8 v[38:41], v[188:189], v[74:75], 0
	v_mfma_f32_16x16x32_fp8_fp8 v[38:41], v[190:191], v[82:83], v[38:41]
	v_mfma_f32_16x16x32_fp8_fp8 v[38:41], v[192:193], v[76:77], v[38:41]
	v_mfma_f32_16x16x32_fp8_fp8 v[38:41], v[194:195], v[118:119], v[38:41]
	s_waitcnt vmcnt(8)
	v_mfma_f32_16x16x32_fp8_fp8 v[54:57], v[196:197], v[74:75], 0
	v_mfma_f32_16x16x32_fp8_fp8 v[54:57], v[198:199], v[82:83], v[54:57]
	v_mfma_f32_16x16x32_fp8_fp8 v[54:57], v[224:225], v[76:77], v[54:57]
	v_mfma_f32_16x16x32_fp8_fp8 v[54:57], v[226:227], v[118:119], v[54:57]
	s_waitcnt vmcnt(6)
	v_mfma_f32_16x16x32_fp8_fp8 v[66:69], v[228:229], v[74:75], 0
	v_mfma_f32_16x16x32_fp8_fp8 v[66:69], v[230:231], v[82:83], v[66:69]
	v_mfma_f32_16x16x32_fp8_fp8 v[66:69], v[232:233], v[76:77], v[66:69]
	v_mfma_f32_16x16x32_fp8_fp8 v[66:69], v[234:235], v[118:119], v[66:69]
	s_waitcnt vmcnt(4)
	v_mfma_f32_16x16x32_fp8_fp8 v[248:251], v[236:237], v[74:75], 0
	v_mfma_f32_16x16x32_fp8_fp8 v[248:251], v[238:239], v[82:83], v[248:251]
	v_mfma_f32_16x16x32_fp8_fp8 v[74:77], v[240:241], v[76:77], v[248:251]
	v_mfma_f32_16x16x32_fp8_fp8 v[74:77], v[242:243], v[118:119], v[74:77]
	s_nop 7
	ds_read2_b64 v[82:85], v121 offset0:56 offset1:60
	v_lshl_add_u32 v140, v120, 2, s22
	s_waitcnt lgkmcnt(0)
	s_cmpk_lt_i32 s97, 0xff
	s_mov_b64 s[8:9], -1
	s_cbranch_scc1 .Lcold_qk

.Lcold_ovf:
	v_and_b32_e32 v3, 64, v209
	v_add_u32_e32 v8, 64, v3
	v_xor_b32_e32 v3, 1, v209
	v_cmp_lt_i32_e32 vcc, v3, v8
	v_xor_b32_e32 v4, 2, v209
	v_xor_b32_e32 v5, 4, v209
	v_cndmask_b32_e32 v3, v209, v3, vcc
	v_cmp_lt_i32_e32 vcc, v4, v8
	v_xor_b32_e32 v6, 8, v209
	v_xor_b32_e32 v7, 16, v209
	v_cndmask_b32_e32 v4, v209, v4, vcc
	v_cmp_lt_i32_e32 vcc, v5, v8
	v_xor_b32_e32 v9, 32, v209
	v_mov_b32_e32 v2, 0
	v_cndmask_b32_e32 v5, v209, v5, vcc
	v_cmp_lt_i32_e32 vcc, v6, v8
	v_lshlrev_b32_e32 v3, 2, v3
	v_lshlrev_b32_e32 v4, 2, v4
	v_cndmask_b32_e32 v6, v209, v6, vcc
	v_cmp_lt_i32_e32 vcc, v7, v8
	v_lshlrev_b32_e32 v5, 2, v5
	v_lshlrev_b32_e32 v6, 2, v6
	v_cndmask_b32_e32 v7, v209, v7, vcc
	v_cmp_lt_i32_e32 vcc, v9, v8
	v_lshlrev_b32_e32 v7, 2, v7
	s_mov_b32 s0, 15
	v_cndmask_b32_e32 v8, v209, v9, vcc
	v_lshlrev_b32_e32 v8, 2, v8
	s_branch .LBB0_743

.Lcold_qk:
	v_cmp_ge_i32_e32 vcc, s10, v117
	v_mov_b32_e32 v119, 0xff800000
	v_mov_b32_e32 v118, 0xff800000
	s_and_saveexec_b64 s[8:9], vcc
	s_cbranch_execz .LBB0_1205
	s_waitcnt lgkmcnt(7)
	v_sub_u32_sdwa v118, s97, v110 dst_sel:DWORD dst_unused:UNUSED_PAD src0_sel:DWORD src1_sel:WORD_0
	v_min_i32_e32 v118, 0x71, v118
	v_lshl_add_u32 v118, v118, 5, v140
	ds_read_b32 v118, v118
	s_waitcnt lgkmcnt(0)
	v_fmac_f32_e32 v118, 0x3e000000, v30

.LBB0_1331:
	s_or_b64 exec, exec, s[8:9]
	v_max3_f32 v215, v118, s23, v119
	v_max3_f32 v215, v215, v120, v121
	v_max3_f32 v215, v215, v122, v123
	v_max3_f32 v215, v215, v124, v125
	v_max3_f32 v215, v215, v126, v127
	v_max3_f32 v215, v215, v128, v129
	v_max3_f32 v215, v215, v130, v131
	v_max3_f32 v215, v215, v132, v133
	v_max3_f32 v215, v215, v134, v135
	v_max3_f32 v215, v215, v136, v137
	v_max3_f32 v215, v215, v156, v157
	v_max3_f32 v215, v215, v158, v159
	v_max3_f32 v215, v215, v160, v161
	v_max3_f32 v215, v215, v162, v163
	v_max3_f32 v215, v215, v164, v165
	v_max3_f32 v215, v215, v166, v167
	v_max3_f32 v215, v215, v168, v169
	v_max3_f32 v215, v215, v170, v171
	v_max3_f32 v215, v215, v172, v173
	v_max3_f32 v215, v215, v174, v175
	v_max3_f32 v215, v215, v176, v177
	v_max3_f32 v215, v215, v178, v179
	v_max3_f32 v215, v215, v180, v181
	v_max3_f32 v215, v215, v182, v183
	v_max3_f32 v215, v215, v184, v185
	v_max3_f32 v215, v215, v186, v187
	v_max3_f32 v215, v215, v188, v189
	v_max3_f32 v215, v215, v190, v191
	v_max3_f32 v215, v215, v192, v193
	v_max3_f32 v215, v215, v194, v195
	v_max3_f32 v215, v215, v196, v197
	v_max3_f32 v215, v215, v198, v199
	s_mov_b64 s[8:9], 0
	s_branch .LBB0_1332
